# grid barrier: all leaders poll the top generation word directly, per-XCD generation publish removed
# baseline (speedup 1.0000x reference)
; __device__ __forceinline__ unsigned xb_ld(unsigned* p)              { return __hip_atomic_load(p, __ATOMIC_RELAXED, __HIP_MEMORY_SCOPE_AGENT); }
; __device__ __forceinline__ unsigned xb_add(unsigned* p, unsigned v) { return __hip_atomic_fetch_add(p, v, __ATOMIC_RELAXED, __HIP_MEMORY_SCOPE_AGENT); }
; #define XB_SPIN(cond, bar) do { unsigned _sp = 0; while (cond) { __builtin_amdgcn_s_sleep(1); \
;     if ((++_sp & 255u) == 0u) { if (xb_ld(&(bar)[XB_TMO])) break; if (_sp > XB_SPIN_CAP) { atomicAdd(&(bar)[XB_TMO], 1u); break; } } } } while (0)
; __device__ __forceinline__ void xcd_barrier(const XcdBarrier& b) {
;     ...
;         const unsigned old = xb_add(&bar[XB_XSUB(b.x)], 1u);
;         const unsigned gen = old / nloc;
;         if (old + 1u == (gen + 1u) * nloc) {
;             __builtin_amdgcn_fence(__ATOMIC_RELEASE, "agent");
;             asm volatile("s_waitcnt vmcnt(0)" ::: "memory");
;             const unsigned og = xb_add(&bar[XB_TOP], 1u);
;             const unsigned tg = og / nx;
;             if (og + 1u == (tg + 1u) * nx) xb_add(&bar[XB_TOPGEN], 1u);
;             else XB_SPIN(xb_ld(&bar[XB_TOPGEN]) == tg, bar);
;             __builtin_amdgcn_fence(__ATOMIC_ACQUIRE, "agent");
;             xb_add(&bar[XB_XGEN(b.x)], 1u);
;             asm volatile("s_waitcnt vmcnt(0)" ::: "memory");
;         } else {
;             XB_SPIN(xb_ld(&bar[XB_XGEN(b.x)]) == gen, bar);
.LBB0_159:
	s_or_b64 exec, exec, s[12:13]
	v_cvt_f32_u32_e32 v4, v2
	s_waitcnt vmcnt(0)
	v_readfirstlane_b32 s3, v3
	v_sub_u32_e32 v3, 0, v2
	v_rcp_iflag_f32_e32 v4, v4
	v_add_u32_e32 v5, s3, v1
	v_mul_f32_e32 v4, 0x4f7ffffe, v4
	v_cvt_u32_f32_e32 v4, v4
	v_mul_lo_u32 v1, v3, v4
	v_mul_hi_u32 v1, v4, v1
	v_add_u32_e32 v1, v4, v1
	v_mul_hi_u32 v1, v5, v1
	v_mul_lo_u32 v3, v1, v2
	v_sub_u32_e32 v3, v5, v3
	v_add_u32_e32 v4, 1, v1
	v_cmp_ge_u32_e32 vcc, v3, v2
	s_nop 1
	v_cndmask_b32_e32 v1, v1, v4, vcc
	v_sub_u32_e32 v4, v3, v2
	v_cndmask_b32_e32 v3, v3, v4, vcc
	v_add_u32_e32 v4, 1, v1
	v_cmp_ge_u32_e32 vcc, v3, v2
	v_add_u32_e32 v3, 1, v5
	s_nop 0
	v_cndmask_b32_e32 v1, v1, v4, vcc
	v_mul_lo_u32 v4, v2, v1
	v_add_u32_e32 v2, v4, v2
	v_cmp_ne_u32_e32 vcc, v3, v2
	s_and_saveexec_b64 s[10:11], vcc
	s_xor_b64 s[10:11], exec, s[10:11]
	s_cbranch_execz .LBB0_173
	s_waitcnt lgkmcnt(0)
	v_mov_b32_e32 v0, 0x3500
	global_load_dword v0, v0, s[30:31] sc1
	s_add_u32 s14, s30, 0x3500
	s_addc_u32 s15, s31, 0
	s_waitcnt vmcnt(0)
	v_cmp_eq_u32_e32 vcc, v0, v1
	s_and_saveexec_b64 s[12:13], vcc
	s_cbranch_execz .LBB0_172
	s_mov_b32 s3, 1
	s_mov_b64 s[16:17], 0
	v_mov_b32_e32 v0, 0
	s_branch .LBB0_163

; __device__ __forceinline__ unsigned xb_ld(unsigned* p)              { return __hip_atomic_load(p, __ATOMIC_RELAXED, __HIP_MEMORY_SCOPE_AGENT); }
; __device__ __forceinline__ unsigned xb_add(unsigned* p, unsigned v) { return __hip_atomic_fetch_add(p, v, __ATOMIC_RELAXED, __HIP_MEMORY_SCOPE_AGENT); }
; #define XB_SPIN(cond, bar) do { unsigned _sp = 0; while (cond) { __builtin_amdgcn_s_sleep(1); \
;     if ((++_sp & 255u) == 0u) { if (xb_ld(&(bar)[XB_TMO])) break; if (_sp > XB_SPIN_CAP) { atomicAdd(&(bar)[XB_TMO], 1u); break; } } } } while (0)
; __device__ __forceinline__ void xcd_barrier(const XcdBarrier& b) {
;     ...
;             __builtin_amdgcn_fence(__ATOMIC_RELEASE, "agent");
;             asm volatile("s_waitcnt vmcnt(0)" ::: "memory");
;             const unsigned og = xb_add(&bar[XB_TOP], 1u);
;             const unsigned tg = og / nx;
;             if (og + 1u == (tg + 1u) * nx) xb_add(&bar[XB_TOPGEN], 1u);
;             else XB_SPIN(xb_ld(&bar[XB_TOPGEN]) == tg, bar);
;             __builtin_amdgcn_fence(__ATOMIC_ACQUIRE, "agent");
;             xb_add(&bar[XB_XGEN(b.x)], 1u);
;             asm volatile("s_waitcnt vmcnt(0)" ::: "memory");
;         } else {
;             XB_SPIN(xb_ld(&bar[XB_XGEN(b.x)]) == gen, bar);
;             __builtin_amdgcn_fence(__ATOMIC_ACQUIRE, "agent");
;             asm volatile("s_waitcnt vmcnt(0)" ::: "memory");
.LBB0_188:
	s_or_b64 exec, exec, s[10:11]
	s_and_saveexec_b64 s[10:11], s[14:15]
	s_cbranch_execz .LBB0_190
	v_mov_b32_e32 v2, 1
	global_atomic_add v[0:1], v2, off
.LBB0_190:
	s_or_b64 exec, exec, s[10:11]
	s_waitcnt vmcnt(0)
	buffer_inv sc1
	s_waitcnt vmcnt(0)
.LBB0_193:
	s_or_b64 exec, exec, s[6:7]
	s_waitcnt lgkmcnt(0)
	s_barrier

; __device__ __forceinline__ unsigned xb_ld(unsigned* p)              { return __hip_atomic_load(p, __ATOMIC_RELAXED, __HIP_MEMORY_SCOPE_AGENT); }
; __device__ __forceinline__ unsigned xb_add(unsigned* p, unsigned v) { return __hip_atomic_fetch_add(p, v, __ATOMIC_RELAXED, __HIP_MEMORY_SCOPE_AGENT); }
; #define XB_SPIN(cond, bar) do { unsigned _sp = 0; while (cond) { __builtin_amdgcn_s_sleep(1); \
;     if ((++_sp & 255u) == 0u) { if (xb_ld(&(bar)[XB_TMO])) break; if (_sp > XB_SPIN_CAP) { atomicAdd(&(bar)[XB_TMO], 1u); break; } } } } while (0)
; __device__ __forceinline__ void xcd_barrier(const XcdBarrier& b) {
;     ...
;             __builtin_amdgcn_fence(__ATOMIC_RELEASE, "agent");
;             asm volatile("s_waitcnt vmcnt(0)" ::: "memory");
;             const unsigned og = xb_add(&bar[XB_TOP], 1u);
;             const unsigned tg = og / nx;
;             if (og + 1u == (tg + 1u) * nx) xb_add(&bar[XB_TOPGEN], 1u);
;             else XB_SPIN(xb_ld(&bar[XB_TOPGEN]) == tg, bar);
;             __builtin_amdgcn_fence(__ATOMIC_ACQUIRE, "agent");
;             xb_add(&bar[XB_XGEN(b.x)], 1u);
;             asm volatile("s_waitcnt vmcnt(0)" ::: "memory");
;         } else {
;             XB_SPIN(xb_ld(&bar[XB_XGEN(b.x)]) == gen, bar);
;             __builtin_amdgcn_fence(__ATOMIC_ACQUIRE, "agent");
;             asm volatile("s_waitcnt vmcnt(0)" ::: "memory");
.LBB0_353:
	s_or_b64 exec, exec, s[10:11]
	s_and_saveexec_b64 s[10:11], s[14:15]
	s_cbranch_execz .LBB0_355
	v_mov_b32_e32 v2, 1
	global_atomic_add v[0:1], v2, off
.LBB0_355:
	s_or_b64 exec, exec, s[10:11]
	s_waitcnt vmcnt(0)
	buffer_inv sc1
	s_waitcnt vmcnt(0)
.LBB0_358:
	s_or_b64 exec, exec, s[6:7]
	s_waitcnt lgkmcnt(0)
	s_barrier

; __device__ __forceinline__ unsigned xb_ld(unsigned* p)              { return __hip_atomic_load(p, __ATOMIC_RELAXED, __HIP_MEMORY_SCOPE_AGENT); }
; __device__ __forceinline__ unsigned xb_add(unsigned* p, unsigned v) { return __hip_atomic_fetch_add(p, v, __ATOMIC_RELAXED, __HIP_MEMORY_SCOPE_AGENT); }
; #define XB_SPIN(cond, bar) do { unsigned _sp = 0; while (cond) { __builtin_amdgcn_s_sleep(1); \
;     if ((++_sp & 255u) == 0u) { if (xb_ld(&(bar)[XB_TMO])) break; if (_sp > XB_SPIN_CAP) { atomicAdd(&(bar)[XB_TMO], 1u); break; } } } } while (0)
; __device__ __forceinline__ void xcd_barrier(const XcdBarrier& b) {
;     ...
;             __builtin_amdgcn_fence(__ATOMIC_RELEASE, "agent");
;             asm volatile("s_waitcnt vmcnt(0)" ::: "memory");
;             const unsigned og = xb_add(&bar[XB_TOP], 1u);
;             const unsigned tg = og / nx;
;             if (og + 1u == (tg + 1u) * nx) xb_add(&bar[XB_TOPGEN], 1u);
;             else XB_SPIN(xb_ld(&bar[XB_TOPGEN]) == tg, bar);
;             __builtin_amdgcn_fence(__ATOMIC_ACQUIRE, "agent");
;             xb_add(&bar[XB_XGEN(b.x)], 1u);
;             asm volatile("s_waitcnt vmcnt(0)" ::: "memory");
;         } else {
;             XB_SPIN(xb_ld(&bar[XB_XGEN(b.x)]) == gen, bar);
;             __builtin_amdgcn_fence(__ATOMIC_ACQUIRE, "agent");
;             asm volatile("s_waitcnt vmcnt(0)" ::: "memory");
.LBB0_464:
	s_or_b64 exec, exec, s[10:11]
	s_and_saveexec_b64 s[10:11], s[14:15]
	s_cbranch_execz .LBB0_466
	v_mov_b32_e32 v2, 1
	global_atomic_add v[0:1], v2, off
.LBB0_466:
	s_or_b64 exec, exec, s[10:11]
	s_waitcnt vmcnt(0)
	buffer_inv sc1
	s_waitcnt vmcnt(0)
.LBB0_469:
	s_or_b64 exec, exec, s[6:7]
	s_waitcnt lgkmcnt(0)
	s_barrier

; __device__ __forceinline__ unsigned xb_ld(unsigned* p)              { return __hip_atomic_load(p, __ATOMIC_RELAXED, __HIP_MEMORY_SCOPE_AGENT); }
; __device__ __forceinline__ unsigned xb_add(unsigned* p, unsigned v) { return __hip_atomic_fetch_add(p, v, __ATOMIC_RELAXED, __HIP_MEMORY_SCOPE_AGENT); }
; #define XB_SPIN(cond, bar) do { unsigned _sp = 0; while (cond) { __builtin_amdgcn_s_sleep(1); \
;     if ((++_sp & 255u) == 0u) { if (xb_ld(&(bar)[XB_TMO])) break; if (_sp > XB_SPIN_CAP) { atomicAdd(&(bar)[XB_TMO], 1u); break; } } } } while (0)
; __device__ __forceinline__ void xcd_barrier(const XcdBarrier& b) {
;     ...
;             __builtin_amdgcn_fence(__ATOMIC_RELEASE, "agent");
;             asm volatile("s_waitcnt vmcnt(0)" ::: "memory");
;             const unsigned og = xb_add(&bar[XB_TOP], 1u);
;             const unsigned tg = og / nx;
;             if (og + 1u == (tg + 1u) * nx) xb_add(&bar[XB_TOPGEN], 1u);
;             else XB_SPIN(xb_ld(&bar[XB_TOPGEN]) == tg, bar);
;             __builtin_amdgcn_fence(__ATOMIC_ACQUIRE, "agent");
;             xb_add(&bar[XB_XGEN(b.x)], 1u);
;             asm volatile("s_waitcnt vmcnt(0)" ::: "memory");
;         } else {
;             XB_SPIN(xb_ld(&bar[XB_XGEN(b.x)]) == gen, bar);
;             __builtin_amdgcn_fence(__ATOMIC_ACQUIRE, "agent");
;             asm volatile("s_waitcnt vmcnt(0)" ::: "memory");
.LBB0_545:
	s_or_b64 exec, exec, s[10:11]
	s_and_saveexec_b64 s[10:11], s[14:15]
	s_cbranch_execz .LBB0_547
	v_mov_b32_e32 v2, 1
	global_atomic_add v[0:1], v2, off
.LBB0_547:
	s_or_b64 exec, exec, s[10:11]
	s_waitcnt vmcnt(0)
	buffer_inv sc1
	s_waitcnt vmcnt(0)
.LBB0_550:
	s_or_b64 exec, exec, s[6:7]
	s_waitcnt lgkmcnt(0)
	s_barrier

; __device__ __forceinline__ unsigned xb_ld(unsigned* p)              { return __hip_atomic_load(p, __ATOMIC_RELAXED, __HIP_MEMORY_SCOPE_AGENT); }
; __device__ __forceinline__ unsigned xb_add(unsigned* p, unsigned v) { return __hip_atomic_fetch_add(p, v, __ATOMIC_RELAXED, __HIP_MEMORY_SCOPE_AGENT); }
; #define XB_SPIN(cond, bar) do { unsigned _sp = 0; while (cond) { __builtin_amdgcn_s_sleep(1); \
;     if ((++_sp & 255u) == 0u) { if (xb_ld(&(bar)[XB_TMO])) break; if (_sp > XB_SPIN_CAP) { atomicAdd(&(bar)[XB_TMO], 1u); break; } } } } while (0)
; __device__ __forceinline__ void xcd_barrier(const XcdBarrier& b) {
;     ...
;             __builtin_amdgcn_fence(__ATOMIC_RELEASE, "agent");
;             asm volatile("s_waitcnt vmcnt(0)" ::: "memory");
;             const unsigned og = xb_add(&bar[XB_TOP], 1u);
;             const unsigned tg = og / nx;
;             if (og + 1u == (tg + 1u) * nx) xb_add(&bar[XB_TOPGEN], 1u);
;             else XB_SPIN(xb_ld(&bar[XB_TOPGEN]) == tg, bar);
;             __builtin_amdgcn_fence(__ATOMIC_ACQUIRE, "agent");
;             xb_add(&bar[XB_XGEN(b.x)], 1u);
;             asm volatile("s_waitcnt vmcnt(0)" ::: "memory");
;         } else {
;             XB_SPIN(xb_ld(&bar[XB_XGEN(b.x)]) == gen, bar);
;             __builtin_amdgcn_fence(__ATOMIC_ACQUIRE, "agent");
;             asm volatile("s_waitcnt vmcnt(0)" ::: "memory");
.LBB0_624:
	s_or_b64 exec, exec, s[10:11]
	s_and_saveexec_b64 s[10:11], s[14:15]
	s_cbranch_execz .LBB0_626
	v_mov_b32_e32 v2, 1
	global_atomic_add v[0:1], v2, off
.LBB0_626:
	s_or_b64 exec, exec, s[10:11]
	s_waitcnt vmcnt(0)
	buffer_inv sc1
	s_waitcnt vmcnt(0)
.LBB0_629:
	s_or_b64 exec, exec, s[6:7]
	s_waitcnt lgkmcnt(0)
	s_barrier

; __device__ __forceinline__ unsigned xb_ld(unsigned* p)              { return __hip_atomic_load(p, __ATOMIC_RELAXED, __HIP_MEMORY_SCOPE_AGENT); }
; __device__ __forceinline__ unsigned xb_add(unsigned* p, unsigned v) { return __hip_atomic_fetch_add(p, v, __ATOMIC_RELAXED, __HIP_MEMORY_SCOPE_AGENT); }
; #define XB_SPIN(cond, bar) do { unsigned _sp = 0; while (cond) { __builtin_amdgcn_s_sleep(1); \
;     if ((++_sp & 255u) == 0u) { if (xb_ld(&(bar)[XB_TMO])) break; if (_sp > XB_SPIN_CAP) { atomicAdd(&(bar)[XB_TMO], 1u); break; } } } } while (0)
; __device__ __forceinline__ void xcd_barrier(const XcdBarrier& b) {
;     ...
;         const unsigned old = xb_add(&bar[XB_XSUB(b.x)], 1u);
;         const unsigned gen = old / nloc;
;         if (old + 1u == (gen + 1u) * nloc) {
;             __builtin_amdgcn_fence(__ATOMIC_RELEASE, "agent");
;             asm volatile("s_waitcnt vmcnt(0)" ::: "memory");
;             const unsigned og = xb_add(&bar[XB_TOP], 1u);
;             const unsigned tg = og / nx;
;             if (og + 1u == (tg + 1u) * nx) xb_add(&bar[XB_TOPGEN], 1u);
;             else XB_SPIN(xb_ld(&bar[XB_TOPGEN]) == tg, bar);
;             __builtin_amdgcn_fence(__ATOMIC_ACQUIRE, "agent");
;             xb_add(&bar[XB_XGEN(b.x)], 1u);
;             asm volatile("s_waitcnt vmcnt(0)" ::: "memory");
;         } else {
;             XB_SPIN(xb_ld(&bar[XB_XGEN(b.x)]) == gen, bar);
.LBB0_655:
	s_or_b64 exec, exec, s[10:11]
	v_cvt_f32_u32_e32 v4, v2
	s_waitcnt vmcnt(0)
	v_readfirstlane_b32 s3, v3
	v_sub_u32_e32 v3, 0, v2
	v_rcp_iflag_f32_e32 v4, v4
	v_add_u32_e32 v5, s3, v1
	v_mul_f32_e32 v4, 0x4f7ffffe, v4
	v_cvt_u32_f32_e32 v4, v4
	v_mul_lo_u32 v1, v3, v4
	v_mul_hi_u32 v1, v4, v1
	v_add_u32_e32 v1, v4, v1
	v_mul_hi_u32 v1, v5, v1
	v_mul_lo_u32 v3, v1, v2
	v_sub_u32_e32 v3, v5, v3
	v_add_u32_e32 v4, 1, v1
	v_cmp_ge_u32_e32 vcc, v3, v2
	s_nop 1
	v_cndmask_b32_e32 v1, v1, v4, vcc
	v_sub_u32_e32 v4, v3, v2
	v_cndmask_b32_e32 v3, v3, v4, vcc
	v_add_u32_e32 v4, 1, v1
	v_cmp_ge_u32_e32 vcc, v3, v2
	v_add_u32_e32 v3, 1, v5
	s_nop 0
	v_cndmask_b32_e32 v1, v1, v4, vcc
	v_mul_lo_u32 v4, v2, v1
	v_add_u32_e32 v2, v4, v2
	v_cmp_ne_u32_e32 vcc, v3, v2
	s_and_saveexec_b64 s[8:9], vcc
	s_xor_b64 s[8:9], exec, s[8:9]
	s_cbranch_execz .LBB0_669
	s_waitcnt lgkmcnt(0)
	v_mov_b32_e32 v0, 0x3500
	global_load_dword v0, v0, s[30:31] sc1
	s_add_u32 s12, s30, 0x3500
	s_addc_u32 s13, s31, 0
	s_waitcnt vmcnt(0)
	v_cmp_eq_u32_e32 vcc, v0, v1
	s_and_saveexec_b64 s[10:11], vcc
	s_cbranch_execz .LBB0_668
	s_mov_b32 s3, 1
	s_mov_b64 s[14:15], 0
	v_mov_b32_e32 v0, 0
	s_branch .LBB0_659

; __device__ __forceinline__ unsigned xb_ld(unsigned* p)              { return __hip_atomic_load(p, __ATOMIC_RELAXED, __HIP_MEMORY_SCOPE_AGENT); }
; __device__ __forceinline__ unsigned xb_add(unsigned* p, unsigned v) { return __hip_atomic_fetch_add(p, v, __ATOMIC_RELAXED, __HIP_MEMORY_SCOPE_AGENT); }
; #define XB_SPIN(cond, bar) do { unsigned _sp = 0; while (cond) { __builtin_amdgcn_s_sleep(1); \
;     if ((++_sp & 255u) == 0u) { if (xb_ld(&(bar)[XB_TMO])) break; if (_sp > XB_SPIN_CAP) { atomicAdd(&(bar)[XB_TMO], 1u); break; } } } } while (0)
; __device__ __forceinline__ void xcd_barrier(const XcdBarrier& b) {
;     ...
;             __builtin_amdgcn_fence(__ATOMIC_ACQUIRE, "agent");
;             xb_add(&bar[XB_XGEN(b.x)], 1u);
;             asm volatile("s_waitcnt vmcnt(0)" ::: "memory");
;         } else {
;             XB_SPIN(xb_ld(&bar[XB_XGEN(b.x)]) == gen, bar);
;             __builtin_amdgcn_fence(__ATOMIC_ACQUIRE, "agent");
;             asm volatile("s_waitcnt vmcnt(0)" ::: "memory");
.LBB0_686:
	s_or_b64 exec, exec, s[8:9]
	s_waitcnt vmcnt(0)
	buffer_inv sc1
	s_waitcnt vmcnt(0)

; __device__ __forceinline__ unsigned xb_ld(unsigned* p)              { return __hip_atomic_load(p, __ATOMIC_RELAXED, __HIP_MEMORY_SCOPE_AGENT); }
; __device__ __forceinline__ unsigned xb_add(unsigned* p, unsigned v) { return __hip_atomic_fetch_add(p, v, __ATOMIC_RELAXED, __HIP_MEMORY_SCOPE_AGENT); }
; #define XB_SPIN(cond, bar) do { unsigned _sp = 0; while (cond) { __builtin_amdgcn_s_sleep(1); \
;     if ((++_sp & 255u) == 0u) { if (xb_ld(&(bar)[XB_TMO])) break; if (_sp > XB_SPIN_CAP) { atomicAdd(&(bar)[XB_TMO], 1u); break; } } } } while (0)
; __device__ __forceinline__ void xcd_barrier(const XcdBarrier& b) {
;     ...
;             __builtin_amdgcn_fence(__ATOMIC_RELEASE, "agent");
;             asm volatile("s_waitcnt vmcnt(0)" ::: "memory");
;             const unsigned og = xb_add(&bar[XB_TOP], 1u);
;             const unsigned tg = og / nx;
;             if (og + 1u == (tg + 1u) * nx) xb_add(&bar[XB_TOPGEN], 1u);
;             else XB_SPIN(xb_ld(&bar[XB_TOPGEN]) == tg, bar);
;             __builtin_amdgcn_fence(__ATOMIC_ACQUIRE, "agent");
;             xb_add(&bar[XB_XGEN(b.x)], 1u);
;             asm volatile("s_waitcnt vmcnt(0)" ::: "memory");
;         } else {
;             XB_SPIN(xb_ld(&bar[XB_XGEN(b.x)]) == gen, bar);
;             __builtin_amdgcn_fence(__ATOMIC_ACQUIRE, "agent");
;             asm volatile("s_waitcnt vmcnt(0)" ::: "memory");
.LBB0_779:
	s_or_b64 exec, exec, s[10:11]
	s_and_saveexec_b64 s[10:11], s[14:15]
	s_cbranch_execz .LBB0_781
	v_mov_b32_e32 v2, 1
	global_atomic_add v[0:1], v2, off
.LBB0_781:
	s_or_b64 exec, exec, s[10:11]
	s_waitcnt vmcnt(0)
	buffer_inv sc1
	s_waitcnt vmcnt(0)
.LBB0_784:
	s_or_b64 exec, exec, s[6:7]
	s_waitcnt lgkmcnt(0)
	s_barrier

; __device__ __forceinline__ unsigned xb_ld(unsigned* p)              { return __hip_atomic_load(p, __ATOMIC_RELAXED, __HIP_MEMORY_SCOPE_AGENT); }
; __device__ __forceinline__ unsigned xb_add(unsigned* p, unsigned v) { return __hip_atomic_fetch_add(p, v, __ATOMIC_RELAXED, __HIP_MEMORY_SCOPE_AGENT); }
; #define XB_SPIN(cond, bar) do { unsigned _sp = 0; while (cond) { __builtin_amdgcn_s_sleep(1); \
;     if ((++_sp & 255u) == 0u) { if (xb_ld(&(bar)[XB_TMO])) break; if (_sp > XB_SPIN_CAP) { atomicAdd(&(bar)[XB_TMO], 1u); break; } } } } while (0)
; __device__ __forceinline__ void xcd_barrier(const XcdBarrier& b) {
;     ...
;             __builtin_amdgcn_fence(__ATOMIC_RELEASE, "agent");
;             asm volatile("s_waitcnt vmcnt(0)" ::: "memory");
;             const unsigned og = xb_add(&bar[XB_TOP], 1u);
;             const unsigned tg = og / nx;
;             if (og + 1u == (tg + 1u) * nx) xb_add(&bar[XB_TOPGEN], 1u);
;             else XB_SPIN(xb_ld(&bar[XB_TOPGEN]) == tg, bar);
;             __builtin_amdgcn_fence(__ATOMIC_ACQUIRE, "agent");
;             xb_add(&bar[XB_XGEN(b.x)], 1u);
;             asm volatile("s_waitcnt vmcnt(0)" ::: "memory");
;         } else {
;             XB_SPIN(xb_ld(&bar[XB_XGEN(b.x)]) == gen, bar);
;             __builtin_amdgcn_fence(__ATOMIC_ACQUIRE, "agent");
;             asm volatile("s_waitcnt vmcnt(0)" ::: "memory");
.LBB0_864:
	s_or_b64 exec, exec, s[10:11]
	s_and_saveexec_b64 s[10:11], s[14:15]
	s_cbranch_execz .LBB0_866
	v_mov_b32_e32 v2, 1
	global_atomic_add v[0:1], v2, off
.LBB0_866:
	s_or_b64 exec, exec, s[10:11]
	s_waitcnt vmcnt(0)
	buffer_inv sc1
	s_waitcnt vmcnt(0)
.LBB0_869:
	s_or_b64 exec, exec, s[6:7]
	s_waitcnt lgkmcnt(0)
	s_barrier

; __device__ __forceinline__ unsigned xb_ld(unsigned* p)              { return __hip_atomic_load(p, __ATOMIC_RELAXED, __HIP_MEMORY_SCOPE_AGENT); }
; __device__ __forceinline__ unsigned xb_add(unsigned* p, unsigned v) { return __hip_atomic_fetch_add(p, v, __ATOMIC_RELAXED, __HIP_MEMORY_SCOPE_AGENT); }
; #define XB_SPIN(cond, bar) do { unsigned _sp = 0; while (cond) { __builtin_amdgcn_s_sleep(1); \
;     if ((++_sp & 255u) == 0u) { if (xb_ld(&(bar)[XB_TMO])) break; if (_sp > XB_SPIN_CAP) { atomicAdd(&(bar)[XB_TMO], 1u); break; } } } } while (0)
; __device__ __forceinline__ void xcd_barrier(const XcdBarrier& b) {
;     ...
;             __builtin_amdgcn_fence(__ATOMIC_RELEASE, "agent");
;             asm volatile("s_waitcnt vmcnt(0)" ::: "memory");
;             const unsigned og = xb_add(&bar[XB_TOP], 1u);
;             const unsigned tg = og / nx;
;             if (og + 1u == (tg + 1u) * nx) xb_add(&bar[XB_TOPGEN], 1u);
;             else XB_SPIN(xb_ld(&bar[XB_TOPGEN]) == tg, bar);
;             __builtin_amdgcn_fence(__ATOMIC_ACQUIRE, "agent");
;             xb_add(&bar[XB_XGEN(b.x)], 1u);
;             asm volatile("s_waitcnt vmcnt(0)" ::: "memory");
;         } else {
;             XB_SPIN(xb_ld(&bar[XB_XGEN(b.x)]) == gen, bar);
;             __builtin_amdgcn_fence(__ATOMIC_ACQUIRE, "agent");
;             asm volatile("s_waitcnt vmcnt(0)" ::: "memory");
.LBB0_924:
	s_or_b64 exec, exec, s[10:11]
	s_and_saveexec_b64 s[10:11], s[14:15]
	s_cbranch_execz .LBB0_926
	v_mov_b32_e32 v2, 1
	global_atomic_add v[0:1], v2, off
.LBB0_926:
	s_or_b64 exec, exec, s[10:11]
	s_waitcnt vmcnt(0)
	buffer_inv sc1
	s_waitcnt vmcnt(0)
.LBB0_929:
	s_or_b64 exec, exec, s[6:7]
	s_waitcnt lgkmcnt(0)
	s_barrier

; __device__ __forceinline__ unsigned xb_ld(unsigned* p)              { return __hip_atomic_load(p, __ATOMIC_RELAXED, __HIP_MEMORY_SCOPE_AGENT); }
; __device__ __forceinline__ unsigned xb_add(unsigned* p, unsigned v) { return __hip_atomic_fetch_add(p, v, __ATOMIC_RELAXED, __HIP_MEMORY_SCOPE_AGENT); }
; #define XB_SPIN(cond, bar) do { unsigned _sp = 0; while (cond) { __builtin_amdgcn_s_sleep(1); \
;     if ((++_sp & 255u) == 0u) { if (xb_ld(&(bar)[XB_TMO])) break; if (_sp > XB_SPIN_CAP) { atomicAdd(&(bar)[XB_TMO], 1u); break; } } } } while (0)
; __device__ __forceinline__ void xcd_barrier(const XcdBarrier& b) {
;     ...
;             __builtin_amdgcn_fence(__ATOMIC_RELEASE, "agent");
;             asm volatile("s_waitcnt vmcnt(0)" ::: "memory");
;             const unsigned og = xb_add(&bar[XB_TOP], 1u);
;             const unsigned tg = og / nx;
;             if (og + 1u == (tg + 1u) * nx) xb_add(&bar[XB_TOPGEN], 1u);
;             else XB_SPIN(xb_ld(&bar[XB_TOPGEN]) == tg, bar);
;             __builtin_amdgcn_fence(__ATOMIC_ACQUIRE, "agent");
;             xb_add(&bar[XB_XGEN(b.x)], 1u);
;             asm volatile("s_waitcnt vmcnt(0)" ::: "memory");
;         } else {
;             XB_SPIN(xb_ld(&bar[XB_XGEN(b.x)]) == gen, bar);
;             __builtin_amdgcn_fence(__ATOMIC_ACQUIRE, "agent");
;             asm volatile("s_waitcnt vmcnt(0)" ::: "memory");
.LBB0_1089:
	s_or_b64 exec, exec, s[10:11]
	s_and_saveexec_b64 s[10:11], s[14:15]
	s_cbranch_execz .LBB0_1091
	v_mov_b32_e32 v2, 1
	global_atomic_add v[0:1], v2, off
.LBB0_1091:
	s_or_b64 exec, exec, s[10:11]
	s_waitcnt vmcnt(0)
	buffer_inv sc1
	s_waitcnt vmcnt(0)
.LBB0_1094:
	s_or_b64 exec, exec, s[6:7]
	s_waitcnt lgkmcnt(0)
	s_barrier

; __device__ __forceinline__ unsigned xb_ld(unsigned* p)              { return __hip_atomic_load(p, __ATOMIC_RELAXED, __HIP_MEMORY_SCOPE_AGENT); }
; __device__ __forceinline__ unsigned xb_add(unsigned* p, unsigned v) { return __hip_atomic_fetch_add(p, v, __ATOMIC_RELAXED, __HIP_MEMORY_SCOPE_AGENT); }
; #define XB_SPIN(cond, bar) do { unsigned _sp = 0; while (cond) { __builtin_amdgcn_s_sleep(1); \
;     if ((++_sp & 255u) == 0u) { if (xb_ld(&(bar)[XB_TMO])) break; if (_sp > XB_SPIN_CAP) { atomicAdd(&(bar)[XB_TMO], 1u); break; } } } } while (0)
; __device__ __forceinline__ void xcd_barrier(const XcdBarrier& b) {
;     ...
;             __builtin_amdgcn_fence(__ATOMIC_RELEASE, "agent");
;             asm volatile("s_waitcnt vmcnt(0)" ::: "memory");
;             const unsigned og = xb_add(&bar[XB_TOP], 1u);
;             const unsigned tg = og / nx;
;             if (og + 1u == (tg + 1u) * nx) xb_add(&bar[XB_TOPGEN], 1u);
;             else XB_SPIN(xb_ld(&bar[XB_TOPGEN]) == tg, bar);
;             __builtin_amdgcn_fence(__ATOMIC_ACQUIRE, "agent");
;             xb_add(&bar[XB_XGEN(b.x)], 1u);
;             asm volatile("s_waitcnt vmcnt(0)" ::: "memory");
;         } else {
;             XB_SPIN(xb_ld(&bar[XB_XGEN(b.x)]) == gen, bar);
;             __builtin_amdgcn_fence(__ATOMIC_ACQUIRE, "agent");
;             asm volatile("s_waitcnt vmcnt(0)" ::: "memory");
.LBB0_1200:
	s_or_b64 exec, exec, s[10:11]
	s_and_saveexec_b64 s[10:11], s[14:15]
	s_cbranch_execz .LBB0_1202
	v_mov_b32_e32 v2, 1
	global_atomic_add v[0:1], v2, off
.LBB0_1202:
	s_or_b64 exec, exec, s[10:11]
	s_waitcnt vmcnt(0)
	buffer_inv sc1
	s_waitcnt vmcnt(0)
.LBB0_1205:
	s_or_b64 exec, exec, s[6:7]
	s_waitcnt lgkmcnt(0)
	s_barrier

; __device__ __forceinline__ unsigned xb_ld(unsigned* p)              { return __hip_atomic_load(p, __ATOMIC_RELAXED, __HIP_MEMORY_SCOPE_AGENT); }
; __device__ __forceinline__ unsigned xb_add(unsigned* p, unsigned v) { return __hip_atomic_fetch_add(p, v, __ATOMIC_RELAXED, __HIP_MEMORY_SCOPE_AGENT); }
; #define XB_SPIN(cond, bar) do { unsigned _sp = 0; while (cond) { __builtin_amdgcn_s_sleep(1); \
;     if ((++_sp & 255u) == 0u) { if (xb_ld(&(bar)[XB_TMO])) break; if (_sp > XB_SPIN_CAP) { atomicAdd(&(bar)[XB_TMO], 1u); break; } } } } while (0)
; __device__ __forceinline__ void xcd_barrier(const XcdBarrier& b) {
;     ...
;             __builtin_amdgcn_fence(__ATOMIC_RELEASE, "agent");
;             asm volatile("s_waitcnt vmcnt(0)" ::: "memory");
;             const unsigned og = xb_add(&bar[XB_TOP], 1u);
;             const unsigned tg = og / nx;
;             if (og + 1u == (tg + 1u) * nx) xb_add(&bar[XB_TOPGEN], 1u);
;             else XB_SPIN(xb_ld(&bar[XB_TOPGEN]) == tg, bar);
;             __builtin_amdgcn_fence(__ATOMIC_ACQUIRE, "agent");
;             xb_add(&bar[XB_XGEN(b.x)], 1u);
;             asm volatile("s_waitcnt vmcnt(0)" ::: "memory");
;         } else {
;             XB_SPIN(xb_ld(&bar[XB_XGEN(b.x)]) == gen, bar);
;             __builtin_amdgcn_fence(__ATOMIC_ACQUIRE, "agent");
;             asm volatile("s_waitcnt vmcnt(0)" ::: "memory");
.LBB0_1281:
	s_or_b64 exec, exec, s[10:11]
	s_and_saveexec_b64 s[10:11], s[14:15]
	s_cbranch_execz .LBB0_1283
	v_mov_b32_e32 v2, 1
	global_atomic_add v[0:1], v2, off
.LBB0_1283:
	s_or_b64 exec, exec, s[10:11]
	s_waitcnt vmcnt(0)
	buffer_inv sc1
	s_waitcnt vmcnt(0)
.LBB0_1286:
	s_or_b64 exec, exec, s[6:7]
	s_waitcnt lgkmcnt(0)
	s_barrier

; __device__ __forceinline__ unsigned xb_ld(unsigned* p)              { return __hip_atomic_load(p, __ATOMIC_RELAXED, __HIP_MEMORY_SCOPE_AGENT); }
; __device__ __forceinline__ unsigned xb_add(unsigned* p, unsigned v) { return __hip_atomic_fetch_add(p, v, __ATOMIC_RELAXED, __HIP_MEMORY_SCOPE_AGENT); }
; #define XB_SPIN(cond, bar) do { unsigned _sp = 0; while (cond) { __builtin_amdgcn_s_sleep(1); \
;     if ((++_sp & 255u) == 0u) { if (xb_ld(&(bar)[XB_TMO])) break; if (_sp > XB_SPIN_CAP) { atomicAdd(&(bar)[XB_TMO], 1u); break; } } } } while (0)
; __device__ __forceinline__ void xcd_barrier(const XcdBarrier& b) {
;     ...
;             __builtin_amdgcn_fence(__ATOMIC_RELEASE, "agent");
;             asm volatile("s_waitcnt vmcnt(0)" ::: "memory");
;             const unsigned og = xb_add(&bar[XB_TOP], 1u);
;             const unsigned tg = og / nx;
;             if (og + 1u == (tg + 1u) * nx) xb_add(&bar[XB_TOPGEN], 1u);
;             else XB_SPIN(xb_ld(&bar[XB_TOPGEN]) == tg, bar);
;             __builtin_amdgcn_fence(__ATOMIC_ACQUIRE, "agent");
;             xb_add(&bar[XB_XGEN(b.x)], 1u);
;             asm volatile("s_waitcnt vmcnt(0)" ::: "memory");
;         } else {
;             XB_SPIN(xb_ld(&bar[XB_XGEN(b.x)]) == gen, bar);
;             __builtin_amdgcn_fence(__ATOMIC_ACQUIRE, "agent");
;             asm volatile("s_waitcnt vmcnt(0)" ::: "memory");
.LBB0_1360:
	s_or_b64 exec, exec, s[10:11]
	s_and_saveexec_b64 s[10:11], s[14:15]
	s_cbranch_execz .LBB0_1362
	v_mov_b32_e32 v2, 1
	global_atomic_add v[0:1], v2, off
.LBB0_1362:
	s_or_b64 exec, exec, s[10:11]
	s_waitcnt vmcnt(0)
	buffer_inv sc1
	s_waitcnt vmcnt(0)
.LBB0_1365:
	s_or_b64 exec, exec, s[6:7]
	s_waitcnt lgkmcnt(0)
	s_barrier

; __device__ __forceinline__ unsigned xb_ld(unsigned* p)              { return __hip_atomic_load(p, __ATOMIC_RELAXED, __HIP_MEMORY_SCOPE_AGENT); }
; __device__ __forceinline__ unsigned xb_add(unsigned* p, unsigned v) { return __hip_atomic_fetch_add(p, v, __ATOMIC_RELAXED, __HIP_MEMORY_SCOPE_AGENT); }
; #define XB_SPIN(cond, bar) do { unsigned _sp = 0; while (cond) { __builtin_amdgcn_s_sleep(1); \
;     if ((++_sp & 255u) == 0u) { if (xb_ld(&(bar)[XB_TMO])) break; if (_sp > XB_SPIN_CAP) { atomicAdd(&(bar)[XB_TMO], 1u); break; } } } } while (0)
; __device__ __forceinline__ void xcd_barrier(const XcdBarrier& b) {
;     ...
;             __builtin_amdgcn_fence(__ATOMIC_RELEASE, "agent");
;             asm volatile("s_waitcnt vmcnt(0)" ::: "memory");
;             const unsigned og = xb_add(&bar[XB_TOP], 1u);
;             const unsigned tg = og / nx;
;             if (og + 1u == (tg + 1u) * nx) xb_add(&bar[XB_TOPGEN], 1u);
;             else XB_SPIN(xb_ld(&bar[XB_TOPGEN]) == tg, bar);
;             __builtin_amdgcn_fence(__ATOMIC_ACQUIRE, "agent");
;             xb_add(&bar[XB_XGEN(b.x)], 1u);
;             asm volatile("s_waitcnt vmcnt(0)" ::: "memory");
;         } else {
;             XB_SPIN(xb_ld(&bar[XB_XGEN(b.x)]) == gen, bar);
;             __builtin_amdgcn_fence(__ATOMIC_ACQUIRE, "agent");
;             asm volatile("s_waitcnt vmcnt(0)" ::: "memory");
.LBB0_1432:
	s_or_b64 exec, exec, s[10:11]
	s_and_saveexec_b64 s[10:11], s[14:15]
	s_cbranch_execz .LBB0_1434
	v_mov_b32_e32 v2, 1
	global_atomic_add v[0:1], v2, off
.LBB0_1434:
	s_or_b64 exec, exec, s[10:11]
	s_waitcnt vmcnt(0)
	buffer_inv sc1
	s_waitcnt vmcnt(0)
.LBB0_1437:
	s_or_b64 exec, exec, s[6:7]
	s_waitcnt lgkmcnt(0)
	s_barrier

; __device__ __forceinline__ unsigned xb_ld(unsigned* p)              { return __hip_atomic_load(p, __ATOMIC_RELAXED, __HIP_MEMORY_SCOPE_AGENT); }
; __device__ __forceinline__ unsigned xb_add(unsigned* p, unsigned v) { return __hip_atomic_fetch_add(p, v, __ATOMIC_RELAXED, __HIP_MEMORY_SCOPE_AGENT); }
; #define XB_SPIN(cond, bar) do { unsigned _sp = 0; while (cond) { __builtin_amdgcn_s_sleep(1); \
;     if ((++_sp & 255u) == 0u) { if (xb_ld(&(bar)[XB_TMO])) break; if (_sp > XB_SPIN_CAP) { atomicAdd(&(bar)[XB_TMO], 1u); break; } } } } while (0)
; __device__ __forceinline__ void xcd_barrier(const XcdBarrier& b) {
;     ...
;             __builtin_amdgcn_fence(__ATOMIC_RELEASE, "agent");
;             asm volatile("s_waitcnt vmcnt(0)" ::: "memory");
;             const unsigned og = xb_add(&bar[XB_TOP], 1u);
;             const unsigned tg = og / nx;
;             if (og + 1u == (tg + 1u) * nx) xb_add(&bar[XB_TOPGEN], 1u);
;             else XB_SPIN(xb_ld(&bar[XB_TOPGEN]) == tg, bar);
;             __builtin_amdgcn_fence(__ATOMIC_ACQUIRE, "agent");
;             xb_add(&bar[XB_XGEN(b.x)], 1u);
;             asm volatile("s_waitcnt vmcnt(0)" ::: "memory");
;         } else {
;             XB_SPIN(xb_ld(&bar[XB_XGEN(b.x)]) == gen, bar);
;             __builtin_amdgcn_fence(__ATOMIC_ACQUIRE, "agent");
;             asm volatile("s_waitcnt vmcnt(0)" ::: "memory");
.LBB0_1588:
	s_or_b64 exec, exec, s[10:11]
	s_and_saveexec_b64 s[10:11], s[14:15]
	s_cbranch_execz .LBB0_1590
	v_mov_b32_e32 v2, 1
	global_atomic_add v[0:1], v2, off
.LBB0_1590:
	s_or_b64 exec, exec, s[10:11]
	s_waitcnt vmcnt(0)
	buffer_inv sc1
	s_waitcnt vmcnt(0)
.LBB0_1593:
	s_or_b64 exec, exec, s[6:7]
	s_waitcnt lgkmcnt(0)
	s_barrier

; __device__ __forceinline__ unsigned xb_ld(unsigned* p)              { return __hip_atomic_load(p, __ATOMIC_RELAXED, __HIP_MEMORY_SCOPE_AGENT); }
; __device__ __forceinline__ unsigned xb_add(unsigned* p, unsigned v) { return __hip_atomic_fetch_add(p, v, __ATOMIC_RELAXED, __HIP_MEMORY_SCOPE_AGENT); }
; #define XB_SPIN(cond, bar) do { unsigned _sp = 0; while (cond) { __builtin_amdgcn_s_sleep(1); \
;     if ((++_sp & 255u) == 0u) { if (xb_ld(&(bar)[XB_TMO])) break; if (_sp > XB_SPIN_CAP) { atomicAdd(&(bar)[XB_TMO], 1u); break; } } } } while (0)
; __device__ __forceinline__ void xcd_barrier(const XcdBarrier& b) {
;     ...
;             __builtin_amdgcn_fence(__ATOMIC_RELEASE, "agent");
;             asm volatile("s_waitcnt vmcnt(0)" ::: "memory");
;             const unsigned og = xb_add(&bar[XB_TOP], 1u);
;             const unsigned tg = og / nx;
;             if (og + 1u == (tg + 1u) * nx) xb_add(&bar[XB_TOPGEN], 1u);
;             else XB_SPIN(xb_ld(&bar[XB_TOPGEN]) == tg, bar);
;             __builtin_amdgcn_fence(__ATOMIC_ACQUIRE, "agent");
;             xb_add(&bar[XB_XGEN(b.x)], 1u);
;             asm volatile("s_waitcnt vmcnt(0)" ::: "memory");
;         } else {
;             XB_SPIN(xb_ld(&bar[XB_XGEN(b.x)]) == gen, bar);
;             __builtin_amdgcn_fence(__ATOMIC_ACQUIRE, "agent");
;             asm volatile("s_waitcnt vmcnt(0)" ::: "memory");
.LBB0_1663:
	s_or_b64 exec, exec, s[10:11]
	s_and_saveexec_b64 s[10:11], s[14:15]
	s_cbranch_execz .LBB0_1665
	v_mov_b32_e32 v2, 1
	global_atomic_add v[0:1], v2, off
.LBB0_1665:
	s_or_b64 exec, exec, s[10:11]
	s_waitcnt vmcnt(0)
	buffer_inv sc1
	s_waitcnt vmcnt(0)
.LBB0_1668:
	s_or_b64 exec, exec, s[6:7]
	s_waitcnt lgkmcnt(0)
	s_barrier

; __device__ __forceinline__ unsigned xb_ld(unsigned* p)              { return __hip_atomic_load(p, __ATOMIC_RELAXED, __HIP_MEMORY_SCOPE_AGENT); }
; __device__ __forceinline__ unsigned xb_add(unsigned* p, unsigned v) { return __hip_atomic_fetch_add(p, v, __ATOMIC_RELAXED, __HIP_MEMORY_SCOPE_AGENT); }
; #define XB_SPIN(cond, bar) do { unsigned _sp = 0; while (cond) { __builtin_amdgcn_s_sleep(1); \
;     if ((++_sp & 255u) == 0u) { if (xb_ld(&(bar)[XB_TMO])) break; if (_sp > XB_SPIN_CAP) { atomicAdd(&(bar)[XB_TMO], 1u); break; } } } } while (0)
; __device__ __forceinline__ void xcd_barrier(const XcdBarrier& b) {
;     ...
;         const unsigned old = xb_add(&bar[XB_XSUB(b.x)], 1u);
;         const unsigned gen = old / nloc;
;         if (old + 1u == (gen + 1u) * nloc) {
;             __builtin_amdgcn_fence(__ATOMIC_RELEASE, "agent");
;             asm volatile("s_waitcnt vmcnt(0)" ::: "memory");
;             const unsigned og = xb_add(&bar[XB_TOP], 1u);
;             const unsigned tg = og / nx;
;             if (og + 1u == (tg + 1u) * nx) xb_add(&bar[XB_TOPGEN], 1u);
;             else XB_SPIN(xb_ld(&bar[XB_TOPGEN]) == tg, bar);
;             __builtin_amdgcn_fence(__ATOMIC_ACQUIRE, "agent");
;             xb_add(&bar[XB_XGEN(b.x)], 1u);
;             asm volatile("s_waitcnt vmcnt(0)" ::: "memory");
;         } else {
;             XB_SPIN(xb_ld(&bar[XB_XGEN(b.x)]) == gen, bar);
.LBB0_1736:
	s_or_b64 exec, exec, s[10:11]
	v_cvt_f32_u32_e32 v4, v2
	s_waitcnt vmcnt(0)
	v_readfirstlane_b32 s8, v3
	v_sub_u32_e32 v3, 0, v2
	v_rcp_iflag_f32_e32 v4, v4
	v_add_u32_e32 v5, s8, v1
	v_mul_f32_e32 v4, 0x4f7ffffe, v4
	v_cvt_u32_f32_e32 v4, v4
	v_mul_lo_u32 v1, v3, v4
	v_mul_hi_u32 v1, v4, v1
	v_add_u32_e32 v1, v4, v1
	v_mul_hi_u32 v1, v5, v1
	v_mul_lo_u32 v3, v1, v2
	v_sub_u32_e32 v3, v5, v3
	v_add_u32_e32 v4, 1, v1
	v_cmp_ge_u32_e32 vcc, v3, v2
	s_nop 1
	v_cndmask_b32_e32 v1, v1, v4, vcc
	v_sub_u32_e32 v4, v3, v2
	v_cndmask_b32_e32 v3, v3, v4, vcc
	v_add_u32_e32 v4, 1, v1
	v_cmp_ge_u32_e32 vcc, v3, v2
	v_add_u32_e32 v3, 1, v5
	s_nop 0
	v_cndmask_b32_e32 v1, v1, v4, vcc
	v_mul_lo_u32 v4, v2, v1
	v_add_u32_e32 v2, v4, v2
	v_cmp_ne_u32_e32 vcc, v3, v2
	s_and_saveexec_b64 s[8:9], vcc
	s_xor_b64 s[8:9], exec, s[8:9]
	s_cbranch_execz .LBB0_1750
	s_waitcnt lgkmcnt(0)
	v_mov_b32_e32 v0, 0x3500
	global_load_dword v0, v0, s[30:31] sc1
	s_add_u32 s12, s30, 0x3500
	s_addc_u32 s13, s31, 0
	s_waitcnt vmcnt(0)
	v_cmp_eq_u32_e32 vcc, v0, v1
	s_and_saveexec_b64 s[10:11], vcc
	s_cbranch_execz .LBB0_1749
	s_mov_b32 s24, 1
	s_mov_b64 s[14:15], 0
	v_mov_b32_e32 v0, 0
	s_branch .LBB0_1740

; __device__ __forceinline__ unsigned xb_ld(unsigned* p)              { return __hip_atomic_load(p, __ATOMIC_RELAXED, __HIP_MEMORY_SCOPE_AGENT); }
; __device__ __forceinline__ unsigned xb_add(unsigned* p, unsigned v) { return __hip_atomic_fetch_add(p, v, __ATOMIC_RELAXED, __HIP_MEMORY_SCOPE_AGENT); }
; #define XB_SPIN(cond, bar) do { unsigned _sp = 0; while (cond) { __builtin_amdgcn_s_sleep(1); \
;     if ((++_sp & 255u) == 0u) { if (xb_ld(&(bar)[XB_TMO])) break; if (_sp > XB_SPIN_CAP) { atomicAdd(&(bar)[XB_TMO], 1u); break; } } } } while (0)
; __device__ __forceinline__ void xcd_barrier(const XcdBarrier& b) {
;     ...
;         const unsigned old = xb_add(&bar[XB_XSUB(b.x)], 1u);
;         const unsigned gen = old / nloc;
;         if (old + 1u == (gen + 1u) * nloc) {
;             __builtin_amdgcn_fence(__ATOMIC_RELEASE, "agent");
;             asm volatile("s_waitcnt vmcnt(0)" ::: "memory");
;             const unsigned og = xb_add(&bar[XB_TOP], 1u);
;             const unsigned tg = og / nx;
;             if (og + 1u == (tg + 1u) * nx) xb_add(&bar[XB_TOPGEN], 1u);
;             else XB_SPIN(xb_ld(&bar[XB_TOPGEN]) == tg, bar);
;             __builtin_amdgcn_fence(__ATOMIC_ACQUIRE, "agent");
;             xb_add(&bar[XB_XGEN(b.x)], 1u);
;             asm volatile("s_waitcnt vmcnt(0)" ::: "memory");
;         } else {
;             XB_SPIN(xb_ld(&bar[XB_XGEN(b.x)]) == gen, bar);
;             __builtin_amdgcn_fence(__ATOMIC_ACQUIRE, "agent");
;             asm volatile("s_waitcnt vmcnt(0)" ::: "memory");
.LBB0_1796:
	s_or_b64 exec, exec, s[6:7]
	v_cvt_f32_u32_e32 v4, v2
	s_waitcnt vmcnt(0)
	v_readfirstlane_b32 s4, v3
	v_sub_u32_e32 v3, 0, v2
	v_rcp_iflag_f32_e32 v4, v4
	v_add_u32_e32 v5, s4, v1
	v_mul_f32_e32 v4, 0x4f7ffffe, v4
	v_cvt_u32_f32_e32 v4, v4
	v_mul_lo_u32 v1, v3, v4
	v_mul_hi_u32 v1, v4, v1
	v_add_u32_e32 v1, v4, v1
	v_mul_hi_u32 v1, v5, v1
	v_mul_lo_u32 v3, v1, v2
	v_sub_u32_e32 v3, v5, v3
	v_add_u32_e32 v4, 1, v1
	v_cmp_ge_u32_e32 vcc, v3, v2
	s_nop 1
	v_cndmask_b32_e32 v1, v1, v4, vcc
	v_sub_u32_e32 v4, v3, v2
	v_cndmask_b32_e32 v3, v3, v4, vcc
	v_add_u32_e32 v4, 1, v1
	v_cmp_ge_u32_e32 vcc, v3, v2
	v_add_u32_e32 v3, 1, v5
	s_nop 0
	v_cndmask_b32_e32 v1, v1, v4, vcc
	v_mul_lo_u32 v4, v2, v1
	v_add_u32_e32 v2, v4, v2
	v_cmp_ne_u32_e32 vcc, v3, v2
	s_and_saveexec_b64 s[4:5], vcc
	s_xor_b64 s[4:5], exec, s[4:5]
	s_cbranch_execz .LBB0_1810
	s_waitcnt lgkmcnt(0)
	v_mov_b32_e32 v0, 0x3500
	global_load_dword v0, v0, s[30:31] sc1
	s_add_u32 s8, s30, 0x3500
	s_addc_u32 s9, s31, 0
	s_waitcnt vmcnt(0)
	v_cmp_eq_u32_e32 vcc, v0, v1
	s_and_saveexec_b64 s[6:7], vcc
	s_cbranch_execz .LBB0_1809
	s_mov_b32 s20, 1
	s_mov_b64 s[10:11], 0
	v_mov_b32_e32 v0, 0
	s_branch .LBB0_1800

; __device__ __forceinline__ unsigned xb_ld(unsigned* p)              { return __hip_atomic_load(p, __ATOMIC_RELAXED, __HIP_MEMORY_SCOPE_AGENT); }
; __device__ __forceinline__ unsigned xb_add(unsigned* p, unsigned v) { return __hip_atomic_fetch_add(p, v, __ATOMIC_RELAXED, __HIP_MEMORY_SCOPE_AGENT); }
; #define XB_SPIN(cond, bar) do { unsigned _sp = 0; while (cond) { __builtin_amdgcn_s_sleep(1); \
;     if ((++_sp & 255u) == 0u) { if (xb_ld(&(bar)[XB_TMO])) break; if (_sp > XB_SPIN_CAP) { atomicAdd(&(bar)[XB_TMO], 1u); break; } } } } while (0)
; __device__ __forceinline__ void xcd_barrier(const XcdBarrier& b) {
;     ...
;             if (og + 1u == (tg + 1u) * nx) xb_add(&bar[XB_TOPGEN], 1u);
;             else XB_SPIN(xb_ld(&bar[XB_TOPGEN]) == tg, bar);
;             __builtin_amdgcn_fence(__ATOMIC_ACQUIRE, "agent");
;             xb_add(&bar[XB_XGEN(b.x)], 1u);
;             asm volatile("s_waitcnt vmcnt(0)" ::: "memory");
;         } else {
;             XB_SPIN(xb_ld(&bar[XB_XGEN(b.x)]) == gen, bar);
;             __builtin_amdgcn_fence(__ATOMIC_ACQUIRE, "agent");
;             asm volatile("s_waitcnt vmcnt(0)" ::: "memory");
.LBB0_1827:
	s_or_b64 exec, exec, s[4:5]
	s_waitcnt vmcnt(0)
	buffer_inv sc1
	s_waitcnt vmcnt(0)
